# v34 + grid barrier between the down / mixer-out GEMM and the thin pass replaced by per-token-tile arrival counters (4 producers per tile)
# baseline (speedup 1.0000x reference)
; __device__ __forceinline__ unsigned xb_ld(unsigned* p)              { return __hip_atomic_load(p, __ATOMIC_RELAXED, __HIP_MEMORY_SCOPE_AGENT); }
; __device__ __forceinline__ unsigned xb_add(unsigned* p, unsigned v) { return __hip_atomic_fetch_add(p, v, __ATOMIC_RELAXED, __HIP_MEMORY_SCOPE_AGENT); }
; #define XB_SPIN(cond, bar) do { unsigned _sp = 0; while (cond) { __builtin_amdgcn_s_sleep(1); \
;     if ((++_sp & 255u) == 0u) { if (xb_ld(&(bar)[XB_TMO])) break; if (_sp > XB_SPIN_CAP) { atomicAdd(&(bar)[XB_TMO], 1u); break; } } } } while (0)
; __device__ __forceinline__ void xcd_barrier(const XcdBarrier& b) {
;     asm volatile("s_waitcnt vmcnt(0)" ::: "memory");
;     __syncthreads();
;     if (threadIdx.x == 0) {
;         unsigned* bar = b.bar;
;         __builtin_amdgcn_s_waitcnt(0);
;         unsigned nloc = b.st[0], nx = b.st[1];
;         if (nloc == 0u) { xcd_barrier_complete(bar, b.x, nloc, nx); b.st[0] = nloc; b.st[1] = nx; }
;         const unsigned old = xb_add(&bar[XB_XSUB(b.x)], 1u);
;         const unsigned gen = old / nloc;
;         if (old + 1u == (gen + 1u) * nloc) {
;             __builtin_amdgcn_fence(__ATOMIC_RELEASE, "agent");
;             asm volatile("s_waitcnt vmcnt(0)" ::: "memory");
;             const unsigned og = xb_add(&bar[XB_TOP], 1u);
;             const unsigned tg = og / nx;
;             if (og + 1u == (tg + 1u) * nx) xb_add(&bar[XB_TOPGEN], 1u);
;             else XB_SPIN(xb_ld(&bar[XB_TOPGEN]) == tg, bar);
;             __builtin_amdgcn_fence(__ATOMIC_ACQUIRE, "agent");
;             xb_add(&bar[XB_XGEN(b.x)], 1u);
;             asm volatile("s_waitcnt vmcnt(0)" ::: "memory");
;         } else {
;             XB_SPIN(xb_ld(&bar[XB_XGEN(b.x)]) == gen, bar);
;             __builtin_amdgcn_fence(__ATOMIC_ACQUIRE, "agent");
;             asm volatile("s_waitcnt vmcnt(0)" ::: "memory");
;         }
;     }
;     __syncthreads();
; }
.LBB0_676:
	v_readlane_b32 s0, v253, 42
	v_readlane_b32 s4, v253, 32
	s_add_i32 s0, s0, 2
	v_readlane_b32 s7, v253, 35
	s_cmp_ge_i32 s0, s7
	v_readlane_b32 s5, v253, 33
	v_readlane_b32 s6, v253, 34
	s_cbranch_scc1 .LBB0_722
	v_readlane_b32 s34, v253, 36
	v_readlane_b32 s35, v253, 37
	s_mov_b32 s1, s76
	s_waitcnt vmcnt(0)
	s_waitcnt vmcnt(0) lgkmcnt(0)
	s_barrier
	s_mov_b64 s[40:41], exec
	v_readlane_b32 s2, v253, 53
	v_readlane_b32 s3, v253, 54
	s_and_b64 s[2:3], s[40:41], s[2:3]
	s_mov_b64 exec, s[2:3]
	s_cbranch_execz .LBB0_721
	v_readlane_b32 s10, v253, 36
	v_readlane_b32 s11, v253, 37
	v_readlane_b32 s14, v253, 55
	s_nop 3
	s_add_u32 s12, s10, 0x4000
	s_addc_u32 s13, s11, 0
	s_and_b32 s15, s88, 7
	s_lshr_b32 s16, s88, 3
	s_lshl_b32 s15, s15, 3
	s_and_b32 s17, s16, 7
	s_add_i32 s17, s17, s15
	s_lshr_b32 s16, s16, 2
	s_add_i32 s16, s16, s15
	s_lshl_b32 s17, s17, 6
	s_lshl_b32 s16, s16, 6
	s_add_i32 s14, s14, 1
	s_lshl_b32 s14, s14, 2
	v_mov_b32_e32 v2, s17
	v_mov_b32_e32 v5, 1
	v_mov_b32_e32 v4, s16
	global_atomic_add v2, v5, s[12:13]
	s_mov_b32 s18, 0
.Lth_poll_LBB0_721:
	global_load_dword v6, v4, s[12:13] sc1
	s_waitcnt vmcnt(0)
	v_cmp_gt_u32_e32 vcc, s14, v6
	s_nop 3
	s_cmp_eq_u64 vcc, 0
	s_cbranch_scc1 .Lth_done_LBB0_721
	s_add_i32 s18, s18, 1
	s_cmp_gt_u32 s18, 0x4000
	s_cbranch_scc1 .Lth_done_LBB0_721
	s_sleep 1
	s_branch .Lth_poll_LBB0_721
.Lth_done_LBB0_721:
	buffer_inv sc1
	s_waitcnt vmcnt(0)

; __device__ __forceinline__ unsigned xb_ld(unsigned* p)              { return __hip_atomic_load(p, __ATOMIC_RELAXED, __HIP_MEMORY_SCOPE_AGENT); }
; __device__ __forceinline__ unsigned xb_add(unsigned* p, unsigned v) { return __hip_atomic_fetch_add(p, v, __ATOMIC_RELAXED, __HIP_MEMORY_SCOPE_AGENT); }
; #define XB_SPIN(cond, bar) do { unsigned _sp = 0; while (cond) { __builtin_amdgcn_s_sleep(1); \
;     if ((++_sp & 255u) == 0u) { if (xb_ld(&(bar)[XB_TMO])) break; if (_sp > XB_SPIN_CAP) { atomicAdd(&(bar)[XB_TMO], 1u); break; } } } } while (0)
; __device__ __forceinline__ void xcd_barrier(const XcdBarrier& b) {
;     asm volatile("s_waitcnt vmcnt(0)" ::: "memory");
;     __syncthreads();
;     if (threadIdx.x == 0) {
;         unsigned* bar = b.bar;
;         __builtin_amdgcn_s_waitcnt(0);
;         unsigned nloc = b.st[0], nx = b.st[1];
;         if (nloc == 0u) { xcd_barrier_complete(bar, b.x, nloc, nx); b.st[0] = nloc; b.st[1] = nx; }
;         const unsigned old = xb_add(&bar[XB_XSUB(b.x)], 1u);
;         const unsigned gen = old / nloc;
;         if (old + 1u == (gen + 1u) * nloc) {
;             __builtin_amdgcn_fence(__ATOMIC_RELEASE, "agent");
;             asm volatile("s_waitcnt vmcnt(0)" ::: "memory");
;             const unsigned og = xb_add(&bar[XB_TOP], 1u);
;             const unsigned tg = og / nx;
;             if (og + 1u == (tg + 1u) * nx) xb_add(&bar[XB_TOPGEN], 1u);
;             else XB_SPIN(xb_ld(&bar[XB_TOPGEN]) == tg, bar);
;             __builtin_amdgcn_fence(__ATOMIC_ACQUIRE, "agent");
;             xb_add(&bar[XB_XGEN(b.x)], 1u);
;             asm volatile("s_waitcnt vmcnt(0)" ::: "memory");
;         } else {
;             XB_SPIN(xb_ld(&bar[XB_XGEN(b.x)]) == gen, bar);
;             __builtin_amdgcn_fence(__ATOMIC_ACQUIRE, "agent");
;             asm volatile("s_waitcnt vmcnt(0)" ::: "memory");
;         }
;     }
;     __syncthreads();
; }
.LBB0_1100:
	v_readlane_b32 s0, v253, 42
	v_readlane_b32 s4, v253, 32
	s_add_i32 s0, s0, 6
	v_readlane_b32 s7, v253, 35
	s_cmp_ge_i32 s0, s7
	v_readlane_b32 s5, v253, 33
	v_readlane_b32 s6, v253, 34
	s_cbranch_scc1 .LBB0_1146
	v_readlane_b32 s38, v253, 36
	v_readlane_b32 s39, v253, 37
	s_mov_b32 s1, s76
	s_waitcnt vmcnt(0)
	s_waitcnt vmcnt(0) lgkmcnt(0)
	s_barrier
	s_mov_b64 s[40:41], exec
	v_readlane_b32 s4, v253, 53
	v_readlane_b32 s5, v253, 54
	s_and_b64 s[4:5], s[40:41], s[4:5]
	s_mov_b64 exec, s[4:5]
	s_cbranch_execz .LBB0_1145
	v_readlane_b32 s10, v253, 36
	v_readlane_b32 s11, v253, 37
	v_readlane_b32 s14, v253, 55
	s_nop 3
	s_add_u32 s12, s10, 0x6000
	s_addc_u32 s13, s11, 0
	s_and_b32 s15, s88, 7
	s_lshr_b32 s16, s88, 3
	s_lshl_b32 s15, s15, 3
	s_and_b32 s17, s16, 7
	s_add_i32 s17, s17, s15
	s_lshr_b32 s16, s16, 2
	s_add_i32 s16, s16, s15
	s_lshl_b32 s17, s17, 6
	s_lshl_b32 s16, s16, 6
	s_lshr_b32 s14, s14, 1
	s_add_i32 s14, s14, 1
	s_lshl_b32 s14, s14, 2
	v_mov_b32_e32 v2, s17
	v_mov_b32_e32 v5, 1
	v_mov_b32_e32 v4, s16
	global_atomic_add v2, v5, s[12:13]
	s_mov_b32 s18, 0

; __device__ __forceinline__ unsigned xb_ld(unsigned* p)              { return __hip_atomic_load(p, __ATOMIC_RELAXED, __HIP_MEMORY_SCOPE_AGENT); }
; __device__ __forceinline__ unsigned xb_add(unsigned* p, unsigned v) { return __hip_atomic_fetch_add(p, v, __ATOMIC_RELAXED, __HIP_MEMORY_SCOPE_AGENT); }
; #define XB_SPIN(cond, bar) do { unsigned _sp = 0; while (cond) { __builtin_amdgcn_s_sleep(1); \
;     if ((++_sp & 255u) == 0u) { if (xb_ld(&(bar)[XB_TMO])) break; if (_sp > XB_SPIN_CAP) { atomicAdd(&(bar)[XB_TMO], 1u); break; } } } } while (0)
; __device__ __forceinline__ void xcd_barrier(const XcdBarrier& b) {
;     asm volatile("s_waitcnt vmcnt(0)" ::: "memory");
;     __syncthreads();
;     if (threadIdx.x == 0) {
;         unsigned* bar = b.bar;
;         __builtin_amdgcn_s_waitcnt(0);
;         unsigned nloc = b.st[0], nx = b.st[1];
;         if (nloc == 0u) { xcd_barrier_complete(bar, b.x, nloc, nx); b.st[0] = nloc; b.st[1] = nx; }
;         const unsigned old = xb_add(&bar[XB_XSUB(b.x)], 1u);
;         const unsigned gen = old / nloc;
;         if (old + 1u == (gen + 1u) * nloc) {
;             __builtin_amdgcn_fence(__ATOMIC_RELEASE, "agent");
;             asm volatile("s_waitcnt vmcnt(0)" ::: "memory");
;             const unsigned og = xb_add(&bar[XB_TOP], 1u);
;             const unsigned tg = og / nx;
;             if (og + 1u == (tg + 1u) * nx) xb_add(&bar[XB_TOPGEN], 1u);
;             else XB_SPIN(xb_ld(&bar[XB_TOPGEN]) == tg, bar);
;             __builtin_amdgcn_fence(__ATOMIC_ACQUIRE, "agent");
;             xb_add(&bar[XB_XGEN(b.x)], 1u);
;             asm volatile("s_waitcnt vmcnt(0)" ::: "memory");
;         } else {
;             XB_SPIN(xb_ld(&bar[XB_XGEN(b.x)]) == gen, bar);
;             __builtin_amdgcn_fence(__ATOMIC_ACQUIRE, "agent");
;             asm volatile("s_waitcnt vmcnt(0)" ::: "memory");
;         }
;     }
;     __syncthreads();
; }
.LBB0_1700:
	v_readlane_b32 s0, v253, 42
	v_readlane_b32 s4, v253, 32
	s_add_i32 s0, s0, 8
	v_readlane_b32 s7, v253, 35
	s_cmp_ge_i32 s0, s7
	v_readlane_b32 s5, v253, 33
	v_readlane_b32 s6, v253, 34
	s_cbranch_scc1 .LBB0_1746
	v_readlane_b32 s34, v253, 36
	v_readlane_b32 s35, v253, 37
	s_mov_b32 s1, s76
	s_waitcnt vmcnt(0)
	s_waitcnt vmcnt(0) lgkmcnt(0)
	s_barrier
	s_mov_b64 s[36:37], exec
	v_readlane_b32 s2, v253, 53
	v_readlane_b32 s3, v253, 54
	s_and_b64 s[2:3], s[36:37], s[2:3]
	s_mov_b64 exec, s[2:3]
	s_cbranch_execz .LBB0_1745
	v_readlane_b32 s10, v253, 36
	v_readlane_b32 s11, v253, 37
	v_readlane_b32 s14, v253, 55
	s_nop 3
	s_add_u32 s12, s10, 0x6000
	s_addc_u32 s13, s11, 0
	s_and_b32 s15, s88, 7
	s_lshr_b32 s16, s88, 3
	s_lshl_b32 s15, s15, 3
	s_and_b32 s17, s16, 7
	s_add_i32 s17, s17, s15
	s_lshr_b32 s16, s16, 2
	s_add_i32 s16, s16, s15
	s_lshl_b32 s17, s17, 6
	s_lshl_b32 s16, s16, 6
	s_lshr_b32 s14, s14, 1
	s_add_i32 s14, s14, 1
	s_lshl_b32 s14, s14, 2
	v_mov_b32_e32 v2, s17
	v_mov_b32_e32 v5, 1
	v_mov_b32_e32 v4, s16
	global_atomic_add v2, v5, s[12:13]
	s_mov_b32 s18, 0
